# speedup vs baseline: 1.0159x; 1.0159x over previous
_Z11gemm_kernelILi128ELi192ELi1EEv8GemmArgs:
	s_load_dwordx2 s[4:5], s[0:1], 0x38
	s_addk_i32 s2, 0xe0
	s_mov_b32 s3, 0
	s_lshl_b64 s[6:7], s[2:3], 2
	s_waitcnt lgkmcnt(0)
	s_add_u32 s4, s4, s6
	s_addc_u32 s5, s5, s7
	s_load_dword s8, s[4:5], 0x0
	s_waitcnt lgkmcnt(0)
	s_cmp_lt_i32 s8, 0
	s_cbranch_scc1 .LBB3_4
	s_load_dwordx2 s[6:7], s[0:1], 0x48
	s_load_dwordx2 s[4:5], s[0:1], 0x0
	v_lshlrev_b32_e32 v64, 4, v0
	v_and_b32_e32 v1, 32, v0
	v_bitop3_b32 v1, v64, v1, 48 bitop3:0x6c
	s_and_b32 s2, s8, 0xffff
	v_bfe_u32 v4, v0, 2, 4
	v_lshrrev_b32_e32 v2, 1, v0
	v_lshrrev_b32_e32 v1, 1, v1
	v_lshrrev_b32_e32 v6, 3, v0
	v_and_or_b32 v1, v2, 32, v1
	v_add_u32_e32 v5, s2, v4
	v_and_b32_e32 v7, 48, v6
	s_movk_i32 s10, 0x70
	v_add_lshl_u32 v22, v5, v7, 12
	v_mov_b32_e32 v23, 0
	v_lshlrev_b32_e32 v44, 1, v1
	v_bitop3_b32 v1, v6, s10, 64 bitop3:0xc8
	s_waitcnt lgkmcnt(0)
	v_lshl_add_u64 v[2:3], s[4:5], 0, v[22:23]
	v_mov_b32_e32 v45, v23
	v_add_lshl_u32 v48, v5, v1, 12
	v_mov_b32_e32 v49, v23
	s_lshr_b32 s10, s8, 24
	s_bfe_u32 s9, s8, 0x80010
	v_lshl_add_u64 v[46:47], v[2:3], 0, v[44:45]
	v_lshl_add_u64 v[2:3], s[4:5], 0, v[48:49]
	s_mulk_i32 s10, 0x300
	v_lshl_add_u64 v[50:51], v[2:3], 0, v[44:45]
	s_mul_i32 s8, s9, 0xc0
	v_or_b32_e32 v2, s10, v4
	v_add_u32_e32 v4, s8, v2
	v_or_b32_e32 v2, v4, v7
	v_lshlrev_b32_e32 v52, 12, v2
	v_mov_b32_e32 v53, v23
	v_lshl_add_u64 v[2:3], s[6:7], 0, v[52:53]
	v_add_lshl_u32 v56, v4, v1, 12
	v_mov_b32_e32 v57, v23
	v_lshl_add_u64 v[54:55], v[2:3], 0, v[44:45]
	v_lshl_add_u64 v[2:3], s[6:7], 0, v[56:57]
	v_add_u32_e32 v60, 0x80000, v52
	v_mov_b32_e32 v61, v23
	v_lshl_add_u64 v[58:59], v[2:3], 0, v[44:45]
	v_lshl_add_u64 v[2:3], s[6:7], 0, v[60:61]
	v_lshl_add_u64 v[62:63], v[2:3], 0, v[44:45]
	v_readfirstlane_b32 s16, v0
	s_load_dwordx2 s[0:1], s[0:1], 0x98
	s_lshr_b32 s16, s16, 6
	s_lshl_b32 s16, s16, 10
	v_bfe_u32 v1, v0, 6, 2
	v_lshrrev_b32_e32 v80, 2, v0
	s_add_u32 m0, s16, 0
	s_nop 0
	global_load_lds_dwordx4 v[46:47], off
	s_add_u32 m0, s16, 8192
	s_nop 0
	global_load_lds_dwordx4 v[50:51], off
	s_add_u32 m0, s16, 16384
	s_nop 0
	global_load_lds_dwordx4 v[54:55], off
	s_add_u32 m0, s16, 24576
	s_nop 0
	global_load_lds_dwordx4 v[58:59], off
	s_add_u32 m0, s16, 32768
	s_nop 0
	global_load_lds_dwordx4 v[62:63], off
	s_add_u32 m0, s16, 40832
	s_nop 0
	global_load_lds_dwordx4 v[46:47], off offset:128
	s_add_u32 m0, s16, 49024
	s_nop 0
	global_load_lds_dwordx4 v[50:51], off offset:128
	s_add_u32 m0, s16, 57216
	s_nop 0
	global_load_lds_dwordx4 v[54:55], off offset:128
	s_add_u32 m0, s16, 65408
	s_nop 0
	global_load_lds_dwordx4 v[58:59], off offset:128
	s_add_u32 m0, s16, 73600
	s_nop 0
	global_load_lds_dwordx4 v[62:63], off offset:128
	s_mov_b32 s17, 0
	s_mov_b32 s18, 0xa000
	s_mov_b32 s19, 0x14000
	v_lshlrev_b32_e32 v25, 6, v0
	v_lshlrev_b32_e32 v27, 2, v0
	v_and_b32_e32 v24, 48, v0
	v_and_b32_e32 v25, 0x3c0, v25
	v_and_b32_e32 v27, 32, v27
	v_or_b32_e32 v26, v25, v24
	v_bitop3_b32 v87, v25, v27, v24 bitop3:0x36
	v_or_b32_e32 v24, v44, v60
	v_mov_b32_e32 v25, v23
	v_lshl_add_u64 v[24:25], s[6:7], 0, v[24:25]
	s_mov_b64 s[10:11], 0x100
	v_lshl_add_u64 v[70:71], v[24:25], 0, s[10:11]
	v_or_b32_e32 v24, v56, v44
	v_mov_b32_e32 v25, v23
	v_lshl_add_u64 v[24:25], s[6:7], 0, v[24:25]
	v_lshl_add_u64 v[72:73], v[24:25], 0, s[10:11]
	v_or_b32_e32 v24, v52, v44
	v_mov_b32_e32 v25, v23
	v_lshl_add_u64 v[24:25], s[6:7], 0, v[24:25]
	v_lshl_add_u64 v[74:75], v[24:25], 0, s[10:11]
	v_or_b32_e32 v24, v48, v44
	v_mov_b32_e32 v25, v23
	v_lshl_add_u64 v[24:25], s[4:5], 0, v[24:25]
	v_or_b32_e32 v22, v22, v44
	v_and_b32_e32 v81, 64, v80
	v_mul_u32_u24_e32 v86, 0x1800, v1
	v_lshl_add_u64 v[76:77], v[24:25], 0, s[10:11]
	v_lshl_add_u64 v[24:25], s[4:5], 0, v[22:23]
	v_bitop3_b32 v82, v26, v86, v27 bitop3:0xde
	v_lshlrev_b32_e32 v88, 7, v81
	v_lshl_add_u64 v[78:79], v[24:25], 0, s[10:11]
	s_mov_b64 s[4:5], 0
	v_mov_b32_e32 v22, v23
	v_mov_b32_e32 v24, v23
	v_mov_b32_e32 v25, v23
	v_mov_b32_e32 v50, v23
	v_mov_b32_e32 v51, v23
	v_mov_b32_e32 v52, v23
	v_mov_b32_e32 v54, v23
	v_mov_b32_e32 v55, v23
	v_mov_b32_e32 v56, v23
	v_mov_b32_e32 v58, v23
	v_mov_b32_e32 v59, v23
	v_mov_b32_e32 v60, v23
	v_mov_b32_e32 v66, v23
	v_mov_b32_e32 v67, v23
	v_mov_b32_e32 v68, v23
	v_mov_b32_e32 v69, v23
	v_mov_b32_e32 v62, v23
	v_mov_b32_e32 v63, v23
	v_mov_b32_e32 v64, v23
	v_mov_b32_e32 v65, v23
	v_mov_b32_e32 v42, v23
	v_mov_b32_e32 v43, v23
	v_mov_b32_e32 v44, v23
	v_mov_b32_e32 v46, v23
	v_mov_b32_e32 v47, v23
	v_mov_b32_e32 v48, v23
	v_mov_b32_e32 v30, v23
	v_mov_b32_e32 v31, v23
	v_mov_b32_e32 v32, v23
	v_mov_b32_e32 v33, v23
	v_mov_b32_e32 v34, v23
	v_mov_b32_e32 v35, v23
	v_mov_b32_e32 v36, v23
	v_mov_b32_e32 v37, v23
	v_mov_b32_e32 v38, v23
	v_mov_b32_e32 v39, v23
	v_mov_b32_e32 v40, v23
	v_mov_b32_e32 v41, v23
	v_mov_b32_e32 v26, v23
	v_mov_b32_e32 v27, v23
	v_mov_b32_e32 v28, v23
	v_mov_b32_e32 v29, v23
	s_waitcnt vmcnt(5) lgkmcnt(0)
	s_barrier
	s_nop 0
	s_nop 0
	s_nop 0
	s_nop 0
	s_nop 0
	s_nop 0
